# gdn_scan chain: output stores spread into the gaps of the state update's 16 MFMAs; state-update LDS fragments read into the registers released by the output MFMAs, on top of v88
# speedup vs baseline: 1.0069x; 1.0003x over previous
.LBB0_490:
	s_bitcmp1_b32 s35, 0
	s_cselect_b32 s26, 0xea00, 0
	v_add_u32_e32 v159, s26, v157
	v_add_u32_e32 v190, v159, v155
	ds_read2_b64 v[68:71], v190 offset1:2
	ds_read2_b64 v[84:87], v190 offset0:4 offset1:6
	ds_read2_b64 v[88:91], v190 offset0:8 offset1:10
	ds_read2_b64 v[92:95], v190 offset0:12 offset1:14
	ds_read2_b64 v[96:99], v190 offset0:16 offset1:18
	ds_read2_b64 v[100:103], v190 offset0:20 offset1:22
	ds_read2_b64 v[104:107], v190 offset0:24 offset1:26
	ds_read2_b64 v[108:111], v190 offset0:28 offset1:30
	v_add_u32_e32 v112, 0x2000, v190
	v_add_u32_e32 v182, 0x2000, v190
	v_add_u32_e32 v186, 0x2000, v190
	v_add_u32_e32 v214, 0x2000, v190
	ds_read2_b64 v[112:115], v112 offset0:48 offset1:50
	ds_read2_b64 v[182:185], v182 offset0:52 offset1:54
	ds_read2_b64 v[186:189], v186 offset0:56 offset1:58
	ds_read2_b64 v[214:217], v214 offset0:60 offset1:62
	v_cvt_pk_bf16_f32 v116, v52, v53
	v_cvt_pk_bf16_f32 v117, v54, v55
	v_cvt_pk_bf16_f32 v118, v56, v57
	v_cvt_pk_bf16_f32 v119, v58, v59
	v_cvt_pk_bf16_f32 v120, v60, v61
	v_cvt_pk_bf16_f32 v121, v62, v63
	v_cvt_pk_bf16_f32 v122, v64, v65
	v_cvt_pk_bf16_f32 v123, v66, v67
	v_cvt_pk_bf16_f32 v124, v36, v37
	v_cvt_pk_bf16_f32 v125, v38, v39
	v_cvt_pk_bf16_f32 v126, v40, v41
	v_cvt_pk_bf16_f32 v127, v42, v43
	v_cvt_pk_bf16_f32 v128, v44, v45
	v_cvt_pk_bf16_f32 v129, v46, v47
	v_cvt_pk_bf16_f32 v130, v48, v49
	v_cvt_pk_bf16_f32 v131, v50, v51
	v_cvt_pk_bf16_f32 v132, v20, v21
	v_cvt_pk_bf16_f32 v133, v22, v23
	v_cvt_pk_bf16_f32 v134, v24, v25
	v_cvt_pk_bf16_f32 v135, v26, v27
	v_cvt_pk_bf16_f32 v136, v28, v29
	v_cvt_pk_bf16_f32 v137, v30, v31
	v_cvt_pk_bf16_f32 v138, v32, v33
	v_cvt_pk_bf16_f32 v139, v34, v35
	v_cvt_pk_bf16_f32 v140, v4, v5
	v_cvt_pk_bf16_f32 v141, v6, v7
	v_cvt_pk_bf16_f32 v142, v8, v9
	v_cvt_pk_bf16_f32 v143, v10, v11
	v_cvt_pk_bf16_f32 v144, v12, v13
	v_cvt_pk_bf16_f32 v145, v14, v15
	v_cvt_pk_bf16_f32 v146, v16, v17
	v_cvt_pk_bf16_f32 v147, v18, v19
	s_waitcnt lgkmcnt(4)
	v_mfma_f32_32x32x16_bf16 v[68:83], v[68:71], v[116:119], 0
	v_mfma_f32_32x32x16_bf16 v[68:83], v[84:87], v[120:123], v[68:83]
	v_add_u32_e32 v84, 0x2000, v190
	ds_read2_b64 v[84:87], v84 offset0:32 offset1:34
	v_mfma_f32_32x32x16_bf16 v[68:83], v[88:91], v[124:127], v[68:83]
	v_mfma_f32_32x32x16_bf16 v[68:83], v[92:95], v[128:131], v[68:83]
	v_mfma_f32_32x32x16_bf16 v[68:83], v[96:99], v[132:135], v[68:83]
	v_mfma_f32_32x32x16_bf16 v[68:83], v[100:103], v[136:139], v[68:83]
	v_add_u32_e32 v100, 0x2000, v190
	ds_read2_b64 v[100:103], v100 offset0:36 offset1:38
	v_mfma_f32_32x32x16_bf16 v[68:83], v[104:107], v[140:143], v[68:83]
	v_add_u32_e32 v104, 0x2000, v190
	ds_read2_b64 v[104:107], v104 offset0:40 offset1:42
	v_mfma_f32_32x32x16_bf16 v[68:83], v[108:111], v[144:147], v[68:83]
	v_add_u32_e32 v108, 0x2000, v190
	ds_read2_b64 v[108:111], v108 offset0:44 offset1:46
	v_add_u32_e32 v88, 0x2000, v190
	s_waitcnt lgkmcnt(3)
	v_mfma_f32_32x32x16_bf16 v[84:99], v[84:87], v[116:119], 0
	s_waitcnt lgkmcnt(2)
	v_mfma_f32_32x32x16_bf16 v[84:99], v[100:103], v[120:123], v[84:99]
	s_waitcnt lgkmcnt(1)
	v_mfma_f32_32x32x16_bf16 v[84:99], v[104:107], v[124:127], v[84:99]
	s_waitcnt lgkmcnt(0)
	v_mfma_f32_32x32x16_bf16 v[84:99], v[108:111], v[128:131], v[84:99]
	v_mfma_f32_32x32x16_bf16 v[84:99], v[112:115], v[132:135], v[84:99]
	v_mfma_f32_32x32x16_bf16 v[84:99], v[182:185], v[136:139], v[84:99]
	v_mfma_f32_32x32x16_bf16 v[84:99], v[186:189], v[140:143], v[84:99]
	v_mfma_f32_32x32x16_bf16 v[84:99], v[214:217], v[144:147], v[84:99]
	s_waitcnt vmcnt(32)
	v_mov_b32_e32 v200, v201
	v_sub_f32_e32 v81, v197, v81
	v_sub_f32_e32 v80, v196, v80
	v_sub_f32_e32 v71, v165, v71
	v_sub_f32_e32 v70, v164, v70
	v_sub_f32_e32 v69, v167, v69
	v_sub_f32_e32 v68, v166, v68
	v_cvt_pk_bf16_f32 v106, v80, v81
	s_nop 3
	v_sub_f32_e32 v80, v175, v87
	v_sub_f32_e32 v81, v174, v86
	v_sub_f32_e32 v83, v199, v83
	v_sub_f32_e32 v82, v198, v82
	v_sub_f32_e32 v79, v195, v79
	v_sub_f32_e32 v78, v194, v78
	v_sub_f32_e32 v77, v181, v77
	v_sub_f32_e32 v76, v180, v76
	v_sub_f32_e32 v75, v171, v75
	v_sub_f32_e32 v74, v170, v74
	v_sub_f32_e32 v73, v169, v73
	v_sub_f32_e32 v72, v168, v72
	v_cvt_pk_bf16_f32 v100, v68, v69
	v_cvt_pk_bf16_f32 v101, v70, v71
	v_sub_f32_e32 v68, v179, v91
	v_sub_f32_e32 v69, v178, v90
	v_sub_f32_e32 v70, v177, v89
	v_sub_f32_e32 v71, v176, v88
	v_cvt_pk_bf16_f32 v109, v81, v80
	v_add_u32_e32 v80, 0x4000, v190
	v_cvt_pk_bf16_f32 v102, v72, v73
	v_cvt_pk_bf16_f32 v103, v74, v75
	v_cvt_pk_bf16_f32 v104, v76, v77
	v_cvt_pk_bf16_f32 v105, v78, v79
	v_cvt_pk_bf16_f32 v107, v82, v83
	v_sub_f32_e32 v72, v209, v99
	v_sub_f32_e32 v73, v208, v98
	v_sub_f32_e32 v74, v207, v97
	v_sub_f32_e32 v75, v206, v96
	v_sub_f32_e32 v76, v205, v95
	v_sub_f32_e32 v77, v204, v94
	v_sub_f32_e32 v78, v203, v93
	v_sub_f32_e32 v79, v202, v92
	v_sub_f32_e32 v82, v173, v85
	v_sub_f32_e32 v83, v172, v84
	v_cvt_pk_bf16_f32 v110, v71, v70
	v_cvt_pk_bf16_f32 v111, v69, v68
	ds_read2_b64 v[68:71], v80 offset0:64 offset1:66
	ds_read2_b64 v[84:87], v80 offset0:68 offset1:70
	ds_read2_b64 v[88:91], v80 offset0:72 offset1:74
	ds_read2_b64 v[92:95], v80 offset0:76 offset1:78
	ds_read2_b64 v[96:99], v80 offset0:80 offset1:82
	ds_read2_b64 v[164:167], v80 offset0:84 offset1:86
	ds_read2_b64 v[168:171], v80 offset0:88 offset1:90
	ds_read2_b64 v[172:175], v80 offset0:92 offset1:94
	v_add_u32_e32 v176, 0x6000, v190
	v_add_u32_e32 v180, 0x6000, v190
	v_add_u32_e32 v184, 0x6000, v190
	v_add_u32_e32 v194, 0x6000, v190
	ds_read2_b64 v[176:179], v176 offset0:112 offset1:114
	ds_read2_b64 v[180:183], v180 offset0:116 offset1:118
	ds_read2_b64 v[184:187], v184 offset0:120 offset1:122
	ds_read2_b64 v[194:197], v194 offset0:124 offset1:126
	v_cvt_pk_bf16_f32 v108, v83, v82
	v_cvt_pk_bf16_f32 v112, v79, v78
	v_cvt_pk_bf16_f32 v113, v77, v76
	v_cvt_pk_bf16_f32 v114, v75, v74
	v_cvt_pk_bf16_f32 v115, v73, v72
	s_waitcnt lgkmcnt(11)
	v_mfma_f32_32x32x16_bf16 v[68:83], v[68:71], v[116:119], 0
	s_waitcnt lgkmcnt(10)
	v_mfma_f32_32x32x16_bf16 v[68:83], v[84:87], v[120:123], v[68:83]
	v_add_u32_e32 v84, 0x6000, v190
	ds_read2_b64 v[84:87], v84 offset0:96 offset1:98
	s_waitcnt lgkmcnt(10)
	v_mfma_f32_32x32x16_bf16 v[68:83], v[88:91], v[124:127], v[68:83]
	s_waitcnt lgkmcnt(9)
	v_mfma_f32_32x32x16_bf16 v[68:83], v[92:95], v[128:131], v[68:83]
	s_waitcnt lgkmcnt(8)
	v_mfma_f32_32x32x16_bf16 v[68:83], v[96:99], v[132:135], v[68:83]
	s_waitcnt lgkmcnt(7)
	v_mfma_f32_32x32x16_bf16 v[68:83], v[164:167], v[136:139], v[68:83]
	v_add_u32_e32 v164, 0x6000, v190
	ds_read2_b64 v[164:167], v164 offset0:100 offset1:102
	s_waitcnt lgkmcnt(7)
	v_mfma_f32_32x32x16_bf16 v[68:83], v[168:171], v[140:143], v[68:83]
	v_add_u32_e32 v168, 0x6000, v190
	ds_read2_b64 v[168:171], v168 offset0:104 offset1:106
	s_waitcnt lgkmcnt(7)
	v_mfma_f32_32x32x16_bf16 v[68:83], v[172:175], v[144:147], v[68:83]
	v_add_u32_e32 v172, 0x6000, v190
	ds_read2_b64 v[172:175], v172 offset0:108 offset1:110
	v_add_u32_e32 v88, 0x6000, v190
	s_waitcnt lgkmcnt(3)
	v_mfma_f32_32x32x16_bf16 v[84:99], v[84:87], v[116:119], 0
	v_add_u32_e32 v116, v159, v153
	v_add_u32_e32 v116, 0x8000, v116
	ds_read2_b64 v[116:119], v116 offset0:128 offset1:130
	s_waitcnt lgkmcnt(3)
	v_mfma_f32_32x32x16_bf16 v[84:99], v[164:167], v[120:123], v[84:99]
	v_add_u32_e32 v120, v159, v153
	v_add_u32_e32 v120, 0x8000, v120
	ds_read2_b64 v[120:123], v120 offset0:132 offset1:134
	s_waitcnt lgkmcnt(3)
	v_mfma_f32_32x32x16_bf16 v[84:99], v[168:171], v[124:127], v[84:99]
	v_add_u32_e32 v124, v159, v153
	v_add_u32_e32 v124, 0x8000, v124
	ds_read2_b64 v[124:127], v124 offset0:136 offset1:138
	s_waitcnt lgkmcnt(3)
	v_mfma_f32_32x32x16_bf16 v[84:99], v[172:175], v[128:131], v[84:99]
	v_add_u32_e32 v128, v159, v153
	v_add_u32_e32 v128, 0x8000, v128
	ds_read2_b64 v[128:131], v128 offset0:140 offset1:142
	v_mfma_f32_32x32x16_bf16 v[84:99], v[176:179], v[132:135], v[84:99]
	v_add_u32_e32 v132, v159, v153
	v_add_u32_e32 v132, 0x9000, v132
	ds_read2_b64 v[132:135], v132 offset0:160 offset1:162
	v_mfma_f32_32x32x16_bf16 v[84:99], v[180:183], v[136:139], v[84:99]
	v_add_u32_e32 v136, v159, v153
	v_add_u32_e32 v136, 0x9000, v136
	ds_read2_b64 v[136:139], v136 offset0:164 offset1:166
	v_mfma_f32_32x32x16_bf16 v[84:99], v[184:187], v[140:143], v[84:99]
	v_add_u32_e32 v140, v159, v153
	v_add_u32_e32 v140, 0x9000, v140
	ds_read2_b64 v[140:143], v140 offset0:168 offset1:170
	v_mfma_f32_32x32x16_bf16 v[84:99], v[194:197], v[144:147], v[84:99]
	v_add_u32_e32 v144, v159, v153
	v_add_u32_e32 v144, 0x9000, v144
	ds_read2_b64 v[144:147], v144 offset0:172 offset1:174
	v_add_u32_e32 v159, v159, v153
	v_lshl_add_u64 v[182:183], s[6:7], 0, v[162:163]
	s_mov_b32 s26, 0x41a20000
	v_add_co_u32_e32 v218, vcc, s26, v182
	s_nop 1
	v_addc_co_u32_e32 v219, vcc, 0, v183, vcc
	s_mov_b32 s26, 0x41a21000
	v_add_co_u32_e32 v220, vcc, s26, v182
	s_nop 1
	v_addc_co_u32_e32 v221, vcc, 0, v183, vcc
	s_mov_b32 s26, 0x41a24000
	v_add_co_u32_e32 v222, vcc, s26, v182
	s_nop 1
	v_addc_co_u32_e32 v223, vcc, 0, v183, vcc
	s_mov_b32 s26, 0x41a25000
	v_add_co_u32_e32 v224, vcc, s26, v182
	s_nop 1
	v_addc_co_u32_e32 v225, vcc, 0, v183, vcc
	global_load_dword v166, v[218:219], off
	global_load_dword v167, v[218:219], off offset:2048
	global_load_dword v164, v[220:221], off
	global_load_dword v165, v[220:221], off offset:2048
	global_load_dword v168, v[222:223], off
	global_load_dword v169, v[222:223], off offset:2048
	global_load_dword v170, v[224:225], off
	global_load_dword v171, v[224:225], off offset:2048
	s_mov_b32 s26, 0x41a28000
	v_add_co_u32_e32 v218, vcc, s26, v182
	s_nop 1
	v_addc_co_u32_e32 v219, vcc, 0, v183, vcc
	s_mov_b32 s26, 0x41a29000
	v_add_co_u32_e32 v220, vcc, s26, v182
	s_nop 1
	v_addc_co_u32_e32 v221, vcc, 0, v183, vcc
	s_mov_b32 s26, 0x41a2c000
	v_add_co_u32_e32 v222, vcc, s26, v182
	s_nop 1
	v_addc_co_u32_e32 v223, vcc, 0, v183, vcc
	s_mov_b32 s26, 0x41a2d000
	v_add_co_u32_e32 v224, vcc, s26, v182
	s_nop 1
	v_addc_co_u32_e32 v225, vcc, 0, v183, vcc
	global_load_dword v180, v[218:219], off
	global_load_dword v181, v[218:219], off offset:2048
	global_load_dword v194, v[220:221], off
	global_load_dword v195, v[220:221], off offset:2048
	global_load_dword v196, v[222:223], off
	global_load_dword v197, v[222:223], off offset:2048
	global_load_dword v198, v[224:225], off
	global_load_dword v199, v[224:225], off offset:2048
	s_mov_b32 s26, 0x41a30000
	v_add_co_u32_e32 v218, vcc, s26, v182
	s_nop 1
	v_addc_co_u32_e32 v219, vcc, 0, v183, vcc
	s_mov_b32 s26, 0x41a31000
	v_add_co_u32_e32 v220, vcc, s26, v182
	s_nop 1
	v_addc_co_u32_e32 v221, vcc, 0, v183, vcc
	s_mov_b32 s26, 0x41a34000
	v_add_co_u32_e32 v222, vcc, s26, v182
	s_nop 1
	v_addc_co_u32_e32 v223, vcc, 0, v183, vcc
	s_mov_b32 s26, 0x41a35000
	v_add_co_u32_e32 v224, vcc, s26, v182
	s_nop 1
	v_addc_co_u32_e32 v225, vcc, 0, v183, vcc
	global_load_dword v172, v[218:219], off
	global_load_dword v173, v[218:219], off offset:2048
	global_load_dword v174, v[220:221], off
	global_load_dword v175, v[220:221], off offset:2048
	global_load_dword v176, v[222:223], off
	global_load_dword v177, v[222:223], off offset:2048
	global_load_dword v178, v[224:225], off
	global_load_dword v179, v[224:225], off offset:2048
	s_mov_b32 s26, 0x41a38000
	v_add_co_u32_e32 v218, vcc, s26, v182
	s_nop 1
	v_addc_co_u32_e32 v219, vcc, 0, v183, vcc
	s_mov_b32 s26, 0x41a39000
	v_add_co_u32_e32 v220, vcc, s26, v182
	s_nop 1
	v_addc_co_u32_e32 v221, vcc, 0, v183, vcc
	s_mov_b32 s26, 0x41a3c000
	v_add_co_u32_e32 v222, vcc, s26, v182
	s_nop 1
	v_addc_co_u32_e32 v223, vcc, 0, v183, vcc
	s_mov_b32 s26, 0x41a3d000
	v_add_co_u32_e32 v224, vcc, s26, v182
	s_nop 1
	v_addc_co_u32_e32 v225, vcc, 0, v183, vcc
	global_load_dword v202, v[218:219], off
	global_load_dword v203, v[218:219], off offset:2048
	global_load_dword v204, v[220:221], off
	global_load_dword v205, v[220:221], off offset:2048
	global_load_dword v206, v[222:223], off
	global_load_dword v207, v[222:223], off offset:2048
	global_load_dword v208, v[224:225], off
	global_load_dword v209, v[224:225], off offset:2048
	s_add_i32 s35, s35, 1
	s_add_u32 s26, s6, s28
	s_addc_u32 s27, s7, s29
	v_mov_b64_e32 v[232:233], s[26:27]
	global_load_dword v201, v[232:233], off
	s_waitcnt lgkmcnt(7)
	v_mfma_f32_32x32x16_bf16 v[68:83], v[116:119], v[100:103], v[68:83]
	s_waitcnt lgkmcnt(3)
	v_mfma_f32_32x32x16_bf16 v[84:99], v[132:135], v[100:103], v[84:99]
	v_mfma_f32_32x32x16_bf16 v[68:83], v[120:123], v[104:107], v[68:83]
	s_waitcnt lgkmcnt(2)
	v_mfma_f32_32x32x16_bf16 v[84:99], v[136:139], v[104:107], v[84:99]
	v_mfma_f32_32x32x16_bf16 v[68:83], v[124:127], v[108:111], v[68:83]
	s_waitcnt lgkmcnt(1)
	v_mfma_f32_32x32x16_bf16 v[84:99], v[140:143], v[108:111], v[84:99]
	v_mfma_f32_32x32x16_bf16 v[68:83], v[128:131], v[112:115], v[68:83]
	s_waitcnt lgkmcnt(0)
	v_mfma_f32_32x32x16_bf16 v[84:99], v[144:147], v[112:115], v[84:99]
	v_add_u32_e32 v116, 0xa000, v159
	ds_read2_b64 v[116:119], v116 offset0:192 offset1:194
	v_add_u32_e32 v120, 0xa000, v159
	ds_read2_b64 v[120:123], v120 offset0:196 offset1:198
	v_add_u32_e32 v124, 0xa000, v159
	ds_read2_b64 v[124:127], v124 offset0:200 offset1:202
	v_add_u32_e32 v128, 0xa000, v159
	ds_read2_b64 v[128:131], v128 offset0:204 offset1:206
	v_add_u32_e32 v132, 0xb000, v159
	ds_read2_b64 v[132:135], v132 offset0:224 offset1:226
	v_add_u32_e32 v136, 0xb000, v159
	ds_read2_b64 v[136:139], v136 offset0:228 offset1:230
	v_add_u32_e32 v140, 0xb000, v159
	ds_read2_b64 v[140:143], v140 offset0:232 offset1:234
	v_add_u32_e32 v144, 0xb000, v159
	ds_read2_b64 v[144:147], v144 offset0:236 offset1:238
	v_pk_mul_f32 v[66:67], v[66:67], v[200:201] op_sel_hi:[1,0]
	v_pk_mul_f32 v[64:65], v[64:65], v[200:201] op_sel_hi:[1,0]
	v_pk_mul_f32 v[62:63], v[62:63], v[200:201] op_sel_hi:[1,0]
	v_pk_mul_f32 v[60:61], v[60:61], v[200:201] op_sel_hi:[1,0]
	v_pk_mul_f32 v[58:59], v[58:59], v[200:201] op_sel_hi:[1,0]
	v_pk_mul_f32 v[56:57], v[56:57], v[200:201] op_sel_hi:[1,0]
	v_pk_mul_f32 v[54:55], v[54:55], v[200:201] op_sel_hi:[1,0]
	v_pk_mul_f32 v[52:53], v[52:53], v[200:201] op_sel_hi:[1,0]
	v_pk_mul_f32 v[50:51], v[50:51], v[200:201] op_sel_hi:[1,0]
	v_pk_mul_f32 v[48:49], v[48:49], v[200:201] op_sel_hi:[1,0]
	v_pk_mul_f32 v[46:47], v[46:47], v[200:201] op_sel_hi:[1,0]
	v_pk_mul_f32 v[44:45], v[44:45], v[200:201] op_sel_hi:[1,0]
	v_pk_mul_f32 v[42:43], v[42:43], v[200:201] op_sel_hi:[1,0]
	v_pk_mul_f32 v[40:41], v[40:41], v[200:201] op_sel_hi:[1,0]
	v_pk_mul_f32 v[38:39], v[38:39], v[200:201] op_sel_hi:[1,0]
	v_pk_mul_f32 v[36:37], v[36:37], v[200:201] op_sel_hi:[1,0]
	s_waitcnt lgkmcnt(0)
	v_mfma_f32_32x32x16_bf16 v[52:67], v[116:119], v[100:103], v[52:67]
	s_mov_b32 s26, 0x47200000
	v_add_co_u32_e32 v218, vcc, s26, v182
	s_nop 1
	v_addc_co_u32_e32 v219, vcc, 0, v183, vcc
	global_store_dword v[218:219], v68, off
	global_store_dword v[218:219], v69, off offset:2048
	v_mfma_f32_32x32x16_bf16 v[36:51], v[132:135], v[100:103], v[36:51]
	s_mov_b32 s26, 0x47201000
	v_add_co_u32_e32 v220, vcc, s26, v182
	s_nop 1
	v_addc_co_u32_e32 v221, vcc, 0, v183, vcc
	global_store_dword v[220:221], v70, off
	global_store_dword v[220:221], v71, off offset:2048
	v_mfma_f32_32x32x16_bf16 v[52:67], v[120:123], v[104:107], v[52:67]
	s_mov_b32 s26, 0x47204000
	v_add_co_u32_e32 v222, vcc, s26, v182
	s_nop 1
	v_addc_co_u32_e32 v223, vcc, 0, v183, vcc
	global_store_dword v[222:223], v72, off
	global_store_dword v[222:223], v73, off offset:2048
	v_mfma_f32_32x32x16_bf16 v[36:51], v[136:139], v[104:107], v[36:51]
	s_mov_b32 s26, 0x47205000
	v_add_co_u32_e32 v224, vcc, s26, v182
	s_nop 1
	v_addc_co_u32_e32 v225, vcc, 0, v183, vcc
	global_store_dword v[224:225], v74, off
	global_store_dword v[224:225], v75, off offset:2048
	v_mfma_f32_32x32x16_bf16 v[52:67], v[124:127], v[108:111], v[52:67]
	s_mov_b32 s26, 0x47208000
	v_add_co_u32_e32 v218, vcc, s26, v182
	s_nop 1
	v_addc_co_u32_e32 v219, vcc, 0, v183, vcc
	global_store_dword v[218:219], v76, off
	global_store_dword v[218:219], v77, off offset:2048
	v_mfma_f32_32x32x16_bf16 v[36:51], v[140:143], v[108:111], v[36:51]
	s_mov_b32 s26, 0x47209000
	v_add_co_u32_e32 v220, vcc, s26, v182
	s_nop 1
	v_addc_co_u32_e32 v221, vcc, 0, v183, vcc
	global_store_dword v[220:221], v78, off
	global_store_dword v[220:221], v79, off offset:2048
	v_mfma_f32_32x32x16_bf16 v[52:67], v[128:131], v[112:115], v[52:67]
	s_mov_b32 s26, 0x4720c000
	v_add_co_u32_e32 v222, vcc, s26, v182
	s_nop 1
	v_addc_co_u32_e32 v223, vcc, 0, v183, vcc
	global_store_dword v[222:223], v80, off
	global_store_dword v[222:223], v81, off offset:2048
	v_mfma_f32_32x32x16_bf16 v[36:51], v[144:147], v[112:115], v[36:51]
	s_mov_b32 s26, 0x4720d000
	v_add_co_u32_e32 v224, vcc, s26, v182
	s_nop 1
	v_addc_co_u32_e32 v225, vcc, 0, v183, vcc
	global_store_dword v[224:225], v82, off
	global_store_dword v[224:225], v83, off offset:2048
	v_add_u32_e32 v116, 0xc800, v159
	ds_read2_b64 v[116:119], v116 offset1:2
	v_add_u32_e32 v120, 0xc800, v159
	ds_read2_b64 v[120:123], v120 offset0:4 offset1:6
	v_add_u32_e32 v124, 0xc800, v159
	ds_read2_b64 v[124:127], v124 offset0:8 offset1:10
	v_add_u32_e32 v128, 0xc800, v159
	ds_read2_b64 v[128:131], v128 offset0:12 offset1:14
	v_add_u32_e32 v132, 0xd800, v159
	ds_read2_b64 v[132:135], v132 offset0:32 offset1:34
	v_add_u32_e32 v136, 0xd800, v159
	ds_read2_b64 v[136:139], v136 offset0:36 offset1:38
	v_add_u32_e32 v140, 0xd800, v159
	ds_read2_b64 v[140:143], v140 offset0:40 offset1:42
	v_add_u32_e32 v144, 0xd800, v159
	ds_read2_b64 v[144:147], v144 offset0:44 offset1:46
	v_pk_mul_f32 v[34:35], v[34:35], v[200:201] op_sel_hi:[1,0]
	v_pk_mul_f32 v[32:33], v[32:33], v[200:201] op_sel_hi:[1,0]
	v_pk_mul_f32 v[30:31], v[30:31], v[200:201] op_sel_hi:[1,0]
	v_pk_mul_f32 v[28:29], v[28:29], v[200:201] op_sel_hi:[1,0]
	v_pk_mul_f32 v[26:27], v[26:27], v[200:201] op_sel_hi:[1,0]
	v_pk_mul_f32 v[24:25], v[24:25], v[200:201] op_sel_hi:[1,0]
	v_pk_mul_f32 v[22:23], v[22:23], v[200:201] op_sel_hi:[1,0]
	v_pk_mul_f32 v[20:21], v[20:21], v[200:201] op_sel_hi:[1,0]
	v_pk_mul_f32 v[18:19], v[18:19], v[200:201] op_sel_hi:[1,0]
	v_pk_mul_f32 v[16:17], v[16:17], v[200:201] op_sel_hi:[1,0]
	v_pk_mul_f32 v[14:15], v[14:15], v[200:201] op_sel_hi:[1,0]
	v_pk_mul_f32 v[12:13], v[12:13], v[200:201] op_sel_hi:[1,0]
	v_pk_mul_f32 v[10:11], v[10:11], v[200:201] op_sel_hi:[1,0]
	v_pk_mul_f32 v[8:9], v[8:9], v[200:201] op_sel_hi:[1,0]
	v_pk_mul_f32 v[6:7], v[6:7], v[200:201] op_sel_hi:[1,0]
	v_pk_mul_f32 v[4:5], v[4:5], v[200:201] op_sel_hi:[1,0]
	s_waitcnt lgkmcnt(0)
	v_mfma_f32_32x32x16_bf16 v[20:35], v[116:119], v[100:103], v[20:35]
	s_mov_b32 s26, 0x47210000
	v_add_co_u32_e32 v218, vcc, s26, v182
	s_nop 1
	v_addc_co_u32_e32 v219, vcc, 0, v183, vcc
	global_store_dword v[218:219], v84, off
	global_store_dword v[218:219], v85, off offset:2048
	v_mfma_f32_32x32x16_bf16 v[4:19], v[132:135], v[100:103], v[4:19]
	s_mov_b32 s26, 0x47211000
	v_add_co_u32_e32 v220, vcc, s26, v182
	s_nop 1
	v_addc_co_u32_e32 v221, vcc, 0, v183, vcc
	global_store_dword v[220:221], v86, off
	global_store_dword v[220:221], v87, off offset:2048
	v_mfma_f32_32x32x16_bf16 v[20:35], v[120:123], v[104:107], v[20:35]
	s_mov_b32 s26, 0x47214000
	v_add_co_u32_e32 v222, vcc, s26, v182
	s_nop 1
	v_addc_co_u32_e32 v223, vcc, 0, v183, vcc
	global_store_dword v[222:223], v88, off
	global_store_dword v[222:223], v89, off offset:2048
	v_mfma_f32_32x32x16_bf16 v[4:19], v[136:139], v[104:107], v[4:19]
	s_mov_b32 s26, 0x47215000
	v_add_co_u32_e32 v224, vcc, s26, v182
	s_nop 1
	v_addc_co_u32_e32 v225, vcc, 0, v183, vcc
	global_store_dword v[224:225], v90, off
	global_store_dword v[224:225], v91, off offset:2048
	v_mfma_f32_32x32x16_bf16 v[20:35], v[124:127], v[108:111], v[20:35]
	s_mov_b32 s26, 0x47218000
	v_add_co_u32_e32 v218, vcc, s26, v182
	s_nop 1
	v_addc_co_u32_e32 v219, vcc, 0, v183, vcc
	global_store_dword v[218:219], v92, off
	global_store_dword v[218:219], v93, off offset:2048
	v_mfma_f32_32x32x16_bf16 v[4:19], v[140:143], v[108:111], v[4:19]
	s_mov_b32 s26, 0x47219000
	v_add_co_u32_e32 v220, vcc, s26, v182
	s_nop 1
	v_addc_co_u32_e32 v221, vcc, 0, v183, vcc
	global_store_dword v[220:221], v94, off
	global_store_dword v[220:221], v95, off offset:2048
	v_mfma_f32_32x32x16_bf16 v[20:35], v[128:131], v[112:115], v[20:35]
	s_mov_b32 s26, 0x4721c000
	v_add_co_u32_e32 v222, vcc, s26, v182
	s_nop 1
	v_addc_co_u32_e32 v223, vcc, 0, v183, vcc
	global_store_dword v[222:223], v96, off
	global_store_dword v[222:223], v97, off offset:2048
	v_mfma_f32_32x32x16_bf16 v[4:19], v[144:147], v[112:115], v[4:19]
	s_mov_b32 s26, 0x4721d000
	v_add_co_u32_e32 v224, vcc, s26, v182
	s_nop 1
	v_addc_co_u32_e32 v225, vcc, 0, v183, vcc
	global_store_dword v[224:225], v98, off
	global_store_dword v[224:225], v99, off offset:2048
	s_add_u32 s28, s28, 4
	s_addc_u32 s29, s29, 0
	v_lshl_add_u64 v[162:163], v[162:163], 0, s[38:39]
	s_cmp_eq_u32 s35, 63
	s_barrier
	s_cbranch_scc0 .LBB0_490
	s_waitcnt vmcnt(32)
	v_add_u32_e32 v82, v157, v155
	v_cvt_pk_bf16_f32 v52, v52, v53
	v_cvt_pk_bf16_f32 v53, v54, v55
	v_cvt_pk_bf16_f32 v54, v56, v57
	v_cvt_pk_bf16_f32 v57, v62, v63
	v_cvt_pk_bf16_f32 v62, v8, v9
	v_add_u32_e32 v8, 0xe800, v82
	v_cvt_pk_bf16_f32 v56, v60, v61
	v_cvt_pk_bf16_f32 v36, v36, v37
	v_cvt_pk_bf16_f32 v37, v38, v39
	v_cvt_pk_bf16_f32 v38, v40, v41
	v_cvt_pk_bf16_f32 v39, v42, v43
	v_cvt_pk_bf16_f32 v40, v44, v45
	v_cvt_pk_bf16_f32 v41, v46, v47
	v_cvt_pk_bf16_f32 v42, v48, v49
	v_cvt_pk_bf16_f32 v43, v50, v51
	v_cvt_pk_bf16_f32 v44, v20, v21
	v_cvt_pk_bf16_f32 v45, v22, v23
	v_cvt_pk_bf16_f32 v46, v24, v25
	v_cvt_pk_bf16_f32 v47, v26, v27
	v_cvt_pk_bf16_f32 v48, v28, v29
	v_cvt_pk_bf16_f32 v49, v30, v31
	v_cvt_pk_bf16_f32 v50, v32, v33
	v_cvt_pk_bf16_f32 v51, v34, v35
	v_cvt_pk_bf16_f32 v60, v4, v5
	v_cvt_pk_bf16_f32 v61, v6, v7
	ds_read2_b64 v[4:7], v8 offset0:64 offset1:66
	ds_read2_b64 v[20:23], v8 offset0:68 offset1:70
	ds_read2_b64 v[24:27], v8 offset0:72 offset1:74
	ds_read2_b64 v[28:31], v8 offset0:76 offset1:78
	ds_read2_b64 v[32:35], v8 offset0:80 offset1:82
	ds_read2_b64 v[68:71], v8 offset0:84 offset1:86
	ds_read2_b64 v[72:75], v8 offset0:88 offset1:90
	ds_read2_b64 v[78:81], v8 offset0:92 offset1:94
	s_add_u32 s24, s6, s24
	s_addc_u32 s25, s7, s25
	s_add_u32 s24, s24, s9
	s_addc_u32 s25, s25, 0
	v_lshl_add_u64 v[76:77], v[160:161], 2, s[24:25]
	v_cvt_pk_bf16_f32 v55, v58, v59
	v_cvt_pk_bf16_f32 v58, v64, v65
	v_cvt_pk_bf16_f32 v59, v66, v67
	v_cvt_pk_bf16_f32 v63, v10, v11
	v_cvt_pk_bf16_f32 v64, v12, v13
	v_cvt_pk_bf16_f32 v65, v14, v15
	v_cvt_pk_bf16_f32 v66, v16, v17
	v_cvt_pk_bf16_f32 v67, v18, v19
	s_waitcnt lgkmcnt(7)
	v_mfma_f32_32x32x16_bf16 v[4:19], v[4:7], v[52:55], 0
	s_waitcnt lgkmcnt(6)
	v_mfma_f32_32x32x16_bf16 v[4:19], v[20:23], v[56:59], v[4:19]
	s_waitcnt lgkmcnt(5)
	v_mfma_f32_32x32x16_bf16 v[4:19], v[24:27], v[36:39], v[4:19]
	s_waitcnt lgkmcnt(4)
	v_mfma_f32_32x32x16_bf16 v[4:19], v[28:31], v[40:43], v[4:19]
	s_waitcnt lgkmcnt(3)
	v_mfma_f32_32x32x16_bf16 v[4:19], v[32:35], v[44:47], v[4:19]
	s_waitcnt lgkmcnt(2)
	v_mfma_f32_32x32x16_bf16 v[4:19], v[68:71], v[48:51], v[4:19]
	s_waitcnt lgkmcnt(1)
	v_mfma_f32_32x32x16_bf16 v[4:19], v[72:75], v[60:63], v[4:19]
	s_waitcnt lgkmcnt(0)
	v_mfma_f32_32x32x16_bf16 v[4:19], v[78:81], v[64:67], v[4:19]
	v_add_u32_e32 v20, 0x2100, v82
	v_add_u32_e32 v24, 0xe800, v20
	ds_read2_b64 v[20:23], v24 offset0:64 offset1:66
	ds_read2_b64 v[68:71], v24 offset0:68 offset1:70
	ds_read2_b64 v[72:75], v24 offset0:72 offset1:74
	ds_read2_b64 v[78:81], v24 offset0:76 offset1:78
	ds_read2_b64 v[82:85], v24 offset0:80 offset1:82
	ds_read2_b64 v[86:89], v24 offset0:84 offset1:86
	ds_read2_b64 v[90:93], v24 offset0:88 offset1:90
	ds_read2_b64 v[94:97], v24 offset0:92 offset1:94
	s_waitcnt lgkmcnt(7)
	v_mfma_f32_32x32x16_bf16 v[20:35], v[20:23], v[52:55], 0
	s_waitcnt lgkmcnt(6)
	v_mfma_f32_32x32x16_bf16 v[20:35], v[68:71], v[56:59], v[20:35]
	s_waitcnt lgkmcnt(5)
	v_mfma_f32_32x32x16_bf16 v[20:35], v[72:75], v[36:39], v[20:35]
	s_waitcnt lgkmcnt(4)
	v_mfma_f32_32x32x16_bf16 v[20:35], v[78:81], v[40:43], v[20:35]
	s_waitcnt lgkmcnt(3)
	v_mfma_f32_32x32x16_bf16 v[20:35], v[82:85], v[44:47], v[20:35]
	s_waitcnt lgkmcnt(2)
	v_mfma_f32_32x32x16_bf16 v[20:35], v[86:89], v[48:51], v[20:35]
	s_waitcnt lgkmcnt(1)
	v_mfma_f32_32x32x16_bf16 v[20:35], v[90:93], v[60:63], v[20:35]
	s_waitcnt lgkmcnt(0)
	v_mfma_f32_32x32x16_bf16 v[20:35], v[94:97], v[64:67], v[20:35]
	v_add_f32_e64 v4, v166, -v4
	v_add_f32_e64 v5, v167, -v5
	v_add_f32_e64 v6, v164, -v6
	v_add_f32_e64 v7, v165, -v7
	v_add_f32_e64 v8, v168, -v8
	v_add_f32_e64 v9, v169, -v9
	v_pk_add_f32 v[10:11], v[170:171], v[10:11] neg_lo:[0,1] neg_hi:[0,1]
	v_pk_add_f32 v[12:13], v[180:181], v[12:13] neg_lo:[0,1] neg_hi:[0,1]
	v_pk_add_f32 v[14:15], v[194:195], v[14:15] neg_lo:[0,1] neg_hi:[0,1]
	v_pk_add_f32 v[16:17], v[196:197], v[16:17] neg_lo:[0,1] neg_hi:[0,1]
	v_pk_add_f32 v[18:19], v[198:199], v[18:19] neg_lo:[0,1] neg_hi:[0,1]
	v_cvt_pk_bf16_f32 v68, v4, v5
	v_cvt_pk_bf16_f32 v69, v6, v7
	v_pk_add_f32 v[4:5], v[172:173], v[20:21] neg_lo:[0,1] neg_hi:[0,1]
	v_pk_add_f32 v[6:7], v[174:175], v[22:23] neg_lo:[0,1] neg_hi:[0,1]
	v_add3_u32 v98, s31, v149, v155
	v_cvt_pk_bf16_f32 v70, v8, v9
	v_cvt_pk_bf16_f32 v71, v10, v11
	v_cvt_pk_bf16_f32 v72, v12, v13
	v_cvt_pk_bf16_f32 v73, v14, v15
	v_cvt_pk_bf16_f32 v74, v16, v17
	v_cvt_pk_bf16_f32 v75, v18, v19
	v_pk_add_f32 v[8:9], v[176:177], v[24:25] neg_lo:[0,1] neg_hi:[0,1]
	v_pk_add_f32 v[10:11], v[178:179], v[26:27] neg_lo:[0,1] neg_hi:[0,1]
	v_pk_add_f32 v[12:13], v[202:203], v[28:29] neg_lo:[0,1] neg_hi:[0,1]
	v_pk_add_f32 v[14:15], v[204:205], v[30:31] neg_lo:[0,1] neg_hi:[0,1]
	v_pk_add_f32 v[16:17], v[206:207], v[32:33] neg_lo:[0,1] neg_hi:[0,1]
	v_pk_add_f32 v[18:19], v[208:209], v[34:35] neg_lo:[0,1] neg_hi:[0,1]
	v_cvt_pk_bf16_f32 v78, v4, v5
	v_cvt_pk_bf16_f32 v79, v6, v7
	ds_read2_b64 v[4:7], v98 offset1:2
	ds_read2_b64 v[20:23], v98 offset0:4 offset1:6
	ds_read2_b64 v[24:27], v98 offset0:8 offset1:10
	ds_read2_b64 v[28:31], v98 offset0:12 offset1:14
	ds_read2_b64 v[32:35], v98 offset0:16 offset1:18
	ds_read2_b64 v[82:85], v98 offset0:20 offset1:22
	ds_read2_b64 v[86:89], v98 offset0:24 offset1:26
	ds_read2_b64 v[90:93], v98 offset0:28 offset1:30
	v_cvt_pk_bf16_f32 v80, v8, v9
	v_cvt_pk_bf16_f32 v81, v10, v11
	v_cvt_pk_bf16_f32 v94, v12, v13
	v_cvt_pk_bf16_f32 v95, v14, v15
	v_cvt_pk_bf16_f32 v96, v16, v17
	v_cvt_pk_bf16_f32 v97, v18, v19
	s_waitcnt lgkmcnt(7)
	v_mfma_f32_32x32x16_bf16 v[4:19], v[4:7], v[52:55], 0
	s_waitcnt lgkmcnt(6)
	v_mfma_f32_32x32x16_bf16 v[4:19], v[20:23], v[56:59], v[4:19]
	s_waitcnt lgkmcnt(5)
	v_mfma_f32_32x32x16_bf16 v[4:19], v[24:27], v[36:39], v[4:19]
	s_waitcnt lgkmcnt(4)
	v_mfma_f32_32x32x16_bf16 v[4:19], v[28:31], v[40:43], v[4:19]
	s_waitcnt lgkmcnt(3)
	v_mfma_f32_32x32x16_bf16 v[4:19], v[32:35], v[44:47], v[4:19]
	s_waitcnt lgkmcnt(2)
	v_mfma_f32_32x32x16_bf16 v[4:19], v[82:85], v[48:51], v[4:19]
	s_waitcnt lgkmcnt(1)
	v_mfma_f32_32x32x16_bf16 v[4:19], v[86:89], v[60:63], v[4:19]
	s_waitcnt lgkmcnt(0)
	v_mfma_f32_32x32x16_bf16 v[4:19], v[90:93], v[64:67], v[4:19]
	v_add_u32_e32 v24, 0x2000, v98
	ds_read2_b64 v[20:23], v24 offset0:32 offset1:34
	ds_read2_b64 v[82:85], v24 offset0:36 offset1:38
	ds_read2_b64 v[86:89], v24 offset0:40 offset1:42
	ds_read2_b64 v[90:93], v24 offset0:44 offset1:46
	ds_read2_b64 v[98:101], v24 offset0:48 offset1:50
	ds_read2_b64 v[102:105], v24 offset0:52 offset1:54
	ds_read2_b64 v[106:109], v24 offset0:56 offset1:58
	ds_read2_b64 v[110:113], v24 offset0:60 offset1:62
	s_waitcnt lgkmcnt(7)
	v_mfma_f32_32x32x16_bf16 v[20:35], v[20:23], v[52:55], 0
	s_waitcnt lgkmcnt(6)
	v_mfma_f32_32x32x16_bf16 v[20:35], v[82:85], v[56:59], v[20:35]
	s_waitcnt lgkmcnt(5)
	v_mfma_f32_32x32x16_bf16 v[20:35], v[86:89], v[36:39], v[20:35]
	s_waitcnt lgkmcnt(4)
	v_mfma_f32_32x32x16_bf16 v[20:35], v[90:93], v[40:43], v[20:35]
	s_waitcnt lgkmcnt(3)
	v_mfma_f32_32x32x16_bf16 v[20:35], v[98:101], v[44:47], v[20:35]
	s_waitcnt lgkmcnt(2)
	v_mfma_f32_32x32x16_bf16 v[20:35], v[102:105], v[48:51], v[20:35]
	s_waitcnt lgkmcnt(1)
	v_mfma_f32_32x32x16_bf16 v[20:35], v[106:109], v[60:63], v[20:35]
	s_waitcnt lgkmcnt(0)
	v_mfma_f32_32x32x16_bf16 v[20:35], v[110:113], v[64:67], v[20:35]
	v_add3_u32 v52, s33, v149, v153
	v_add_u32_e32 v64, 0x1000, v52
	ds_read2_b64 v[36:39], v52 offset1:2
	ds_read2_b64 v[40:43], v52 offset0:4 offset1:6
	ds_read2_b64 v[44:47], v52 offset0:8 offset1:10
	ds_read2_b64 v[48:51], v52 offset0:12 offset1:14
	ds_read2_b64 v[52:55], v64 offset0:32 offset1:34
	ds_read2_b64 v[56:59], v64 offset0:36 offset1:38
	ds_read2_b64 v[60:63], v64 offset0:40 offset1:42
	ds_read2_b64 v[64:67], v64 offset0:44 offset1:46
	s_waitcnt lgkmcnt(7)
	v_mfma_f32_32x32x16_bf16 v[4:19], v[36:39], v[68:71], v[4:19]
	s_waitcnt lgkmcnt(3)
	v_mfma_f32_32x32x16_bf16 v[20:35], v[52:55], v[68:71], v[20:35]
	v_mfma_f32_32x32x16_bf16 v[4:19], v[40:43], v[72:75], v[4:19]
	s_waitcnt lgkmcnt(2)
	v_mfma_f32_32x32x16_bf16 v[20:35], v[56:59], v[72:75], v[20:35]
	v_mfma_f32_32x32x16_bf16 v[4:19], v[44:47], v[78:81], v[4:19]
	s_waitcnt lgkmcnt(1)
	v_mfma_f32_32x32x16_bf16 v[20:35], v[60:63], v[78:81], v[20:35]
	v_mfma_f32_32x32x16_bf16 v[4:19], v[48:51], v[94:97], v[4:19]
	s_waitcnt lgkmcnt(0)
	v_mfma_f32_32x32x16_bf16 v[20:35], v[64:67], v[94:97], v[20:35]
	v_lshl_add_u64 v[36:37], v[76:77], 0, v[2:3]
	s_mov_b32 s9, 0x479e0000
	v_add_co_u32_e32 v38, vcc, s9, v36
	s_mov_b32 s9, 0x479e1000
	s_nop 0
	v_addc_co_u32_e32 v39, vcc, 0, v37, vcc
	s_nop 3
	global_store_dword v[38:39], v4, off
	global_store_dword v[38:39], v5, off offset:2048
	v_add_co_u32_e32 v4, vcc, s9, v36
	s_mov_b32 s9, 0x479e4000
	s_nop 0
	v_addc_co_u32_e32 v5, vcc, 0, v37, vcc
	global_store_dword v[4:5], v6, off
	global_store_dword v[4:5], v7, off offset:2048
	v_add_co_u32_e32 v4, vcc, s9, v36
	s_mov_b32 s9, 0x479e5000
	s_nop 0
	v_addc_co_u32_e32 v5, vcc, 0, v37, vcc
	global_store_dword v[4:5], v8, off
	global_store_dword v[4:5], v9, off offset:2048
	v_add_co_u32_e32 v4, vcc, s9, v36
	s_mov_b32 s9, 0x479e8000
	s_nop 0
	v_addc_co_u32_e32 v5, vcc, 0, v37, vcc
	global_store_dword v[4:5], v10, off
	global_store_dword v[4:5], v11, off offset:2048
	v_add_co_u32_e32 v4, vcc, s9, v36
	s_mov_b32 s9, 0x479e9000
	s_nop 0
	v_addc_co_u32_e32 v5, vcc, 0, v37, vcc
	global_store_dword v[4:5], v12, off
	global_store_dword v[4:5], v13, off offset:2048
	v_add_co_u32_e32 v4, vcc, s9, v36
	s_mov_b32 s9, 0x479ec000
	s_nop 0
	v_addc_co_u32_e32 v5, vcc, 0, v37, vcc
	global_store_dword v[4:5], v14, off
	global_store_dword v[4:5], v15, off offset:2048
	v_add_co_u32_e32 v4, vcc, s9, v36
	s_mov_b32 s9, 0x479ed000
	s_nop 0
	v_addc_co_u32_e32 v5, vcc, 0, v37, vcc
	global_store_dword v[4:5], v16, off
	global_store_dword v[4:5], v17, off offset:2048
	v_add_co_u32_e32 v4, vcc, s9, v36
	s_mov_b32 s9, 0x479f0000
	s_nop 0
	v_addc_co_u32_e32 v5, vcc, 0, v37, vcc
	global_store_dword v[4:5], v18, off
	global_store_dword v[4:5], v19, off offset:2048
	v_add_co_u32_e32 v4, vcc, s9, v36
	s_mov_b32 s9, 0x479f1000
	s_nop 0
	v_addc_co_u32_e32 v5, vcc, 0, v37, vcc
	global_store_dword v[4:5], v20, off
	global_store_dword v[4:5], v21, off offset:2048
	v_add_co_u32_e32 v4, vcc, s9, v36
	s_mov_b32 s9, 0x479f4000
	s_nop 0
	v_addc_co_u32_e32 v5, vcc, 0, v37, vcc
	global_store_dword v[4:5], v22, off
	global_store_dword v[4:5], v23, off offset:2048
	v_add_co_u32_e32 v4, vcc, s9, v36
	s_mov_b32 s9, 0x479f5000
	s_nop 0
	v_addc_co_u32_e32 v5, vcc, 0, v37, vcc
	global_store_dword v[4:5], v24, off
	global_store_dword v[4:5], v25, off offset:2048
	v_add_co_u32_e32 v4, vcc, s9, v36
	s_mov_b32 s9, 0x479f8000
	s_nop 0
	v_addc_co_u32_e32 v5, vcc, 0, v37, vcc
	global_store_dword v[4:5], v26, off
	global_store_dword v[4:5], v27, off offset:2048
	v_add_co_u32_e32 v4, vcc, s9, v36
	s_mov_b32 s9, 0x479f9000
	s_nop 0
	v_addc_co_u32_e32 v5, vcc, 0, v37, vcc
	global_store_dword v[4:5], v28, off
	global_store_dword v[4:5], v29, off offset:2048
	v_add_co_u32_e32 v4, vcc, s9, v36
	s_mov_b32 s9, 0x479fc000
	s_nop 0
	v_addc_co_u32_e32 v5, vcc, 0, v37, vcc
	global_store_dword v[4:5], v30, off
	global_store_dword v[4:5], v31, off offset:2048
	v_add_co_u32_e32 v4, vcc, s9, v36
	s_nop 1
	v_addc_co_u32_e32 v5, vcc, 0, v37, vcc
	global_store_dword v[4:5], v32, off
	global_store_dword v[4:5], v33, off offset:2048
	v_add_co_u32_e32 v4, vcc, 0x479fd000, v36
	s_nop 1
	v_addc_co_u32_e32 v5, vcc, 0, v37, vcc
	global_store_dword v[4:5], v34, off
	global_store_dword v[4:5], v35, off offset:2048
	s_mov_b64 s[28:29], 0
	s_waitcnt lgkmcnt(0)
	s_barrier
